# g4: g2 + mixer chunk loops keep next-chunk prefetch in flight (counted vmcnt instead of compiler vmcnt(0) before z-tile use)
# baseline (speedup 1.0000x reference)
.LBB0_231:
	v_add_u32_e32 v242, 0, v217
	ds_read_b128 v[218:221], v242
	ds_read_b128 v[222:225], v242 offset:64
	ds_read_b128 v[226:229], v242 offset:128
	ds_read_b128 v[230:233], v242 offset:192
	v_add_u32_e32 v234, 0, v212
	s_waitcnt lgkmcnt(3)
	v_mfma_f32_16x16x32_bf16 v[218:221], v[218:221], v[66:69], 0
	v_add_u32_e32 v235, 0x22000, v234
	v_add_u32_e32 v238, 0x22400, v234
	v_add_u32_e32 v243, 0x22040, v234
	s_waitcnt lgkmcnt(2)
	v_mfma_f32_16x16x32_bf16 v[218:221], v[222:225], v[70:73], v[218:221]
	v_add_u32_e32 v248, 0x22440, v234
	ds_read_b128 v[234:237], v235
	ds_read_b128 v[238:241], v238
	s_cmp_lt_u32 s50, s82
	s_waitcnt lgkmcnt(3)
	v_mfma_f32_16x16x32_bf16 v[218:221], v[226:229], v[74:77], v[218:221]
	s_cselect_b64 vcc, -1, 0
	s_waitcnt lgkmcnt(1)
	v_sub_f32_e32 v234, v234, v125
	v_sub_f32_e32 v236, v236, v125
	v_sub_f32_e32 v237, v237, v125
	v_mul_f32_e32 v234, 0x3fb8aa3b, v234
	v_mul_f32_e32 v222, 0x3fb8aa3b, v236
	v_mul_f32_e32 v223, 0x3fb8aa3b, v237
	v_sub_f32_e32 v235, v235, v125
	v_exp_f32_e32 v224, v234
	v_exp_f32_e32 v222, v222
	v_exp_f32_e32 v223, v223
	v_mfma_f32_16x16x32_bf16 v[218:221], v[230:233], v[78:81], v[218:221]
	v_mul_f32_e32 v235, 0x3fb8aa3b, v235
	v_exp_f32_e32 v225, v235
	s_cmp_eq_u32 s50, s82
	s_cselect_b64 s[0:1], -1, 0
	s_and_b64 s[52:53], s[0:1], s[20:21]
	s_nop 2
	v_mul_f32_e32 v218, v218, v224
	v_mul_f32_e32 v220, v220, v222
	v_mul_f32_e32 v221, v221, v223
	s_waitcnt lgkmcnt(0)
	v_mul_f32_e32 v218, v238, v218
	v_mul_f32_e32 v220, v240, v220
	v_mul_f32_e32 v221, v241, v221
	v_mul_f32_e32 v219, v219, v225
	v_cndmask_b32_e64 v222, v218, 0, s[18:19]
	v_cndmask_b32_e64 v223, v220, 0, s[22:23]
	v_cndmask_b32_e64 v224, v221, 0, s[24:25]
	v_mul_f32_e32 v219, v239, v219
	v_cndmask_b32_e64 v222, 0, v222, s[0:1]
	v_cndmask_b32_e64 v223, 0, v223, s[0:1]
	v_cndmask_b32_e64 v224, 0, v224, s[0:1]
	s_or_b64 s[0:1], vcc, s[52:53]
	v_cndmask_b32_e32 v218, v222, v218, vcc
	v_cndmask_b32_e64 v219, 0, v219, s[0:1]
	v_cndmask_b32_e32 v220, v223, v220, vcc
	v_cndmask_b32_e32 v221, v224, v221, vcc
	v_cvt_pk_bf16_f32 v218, v218, v219
	s_nop 1
	v_cvt_pk_bf16_f32 v219, v220, v221
	s_nop 1
	ds_read_b128 v[220:223], v242 offset:4352
	ds_read_b128 v[224:227], v242 offset:4416
	ds_read_b128 v[228:231], v243
	ds_read_b128 v[232:235], v242 offset:4480
	ds_read_b128 v[236:239], v242 offset:4544
	ds_read_b128 v[240:243], v248
	s_waitcnt lgkmcnt(5)
	v_mfma_f32_16x16x32_bf16 v[220:223], v[220:223], v[66:69], 0
	s_waitcnt lgkmcnt(3)
	v_sub_f32_e32 v228, v228, v125
	v_sub_f32_e32 v230, v230, v125
	v_sub_f32_e32 v231, v231, v125
	v_mfma_f32_16x16x32_bf16 v[220:223], v[224:227], v[70:73], v[220:223]
	v_mul_f32_e32 v228, 0x3fb8aa3b, v228
	v_mul_f32_e32 v224, 0x3fb8aa3b, v230
	v_mul_f32_e32 v225, 0x3fb8aa3b, v231
	s_waitcnt lgkmcnt(2)
	v_mfma_f32_16x16x32_bf16 v[220:223], v[232:235], v[74:77], v[220:223]
	v_sub_f32_e32 v229, v229, v125
	v_exp_f32_e32 v226, v228
	v_exp_f32_e32 v224, v224
	v_exp_f32_e32 v225, v225
	s_waitcnt lgkmcnt(1)
	v_mfma_f32_16x16x32_bf16 v[220:223], v[236:239], v[78:81], v[220:223]
	v_mul_f32_e32 v229, 0x3fb8aa3b, v229
	s_add_i32 s51, s50, 1
	v_exp_f32_e32 v227, v229
	s_cmp_lt_u32 s51, s82
	s_cselect_b64 vcc, -1, 0
	s_nop 2
	v_mul_f32_e32 v220, v220, v226
	v_mul_f32_e32 v222, v222, v224
	v_mul_f32_e32 v223, v223, v225
	s_cmp_eq_u32 s51, s82
	s_waitcnt lgkmcnt(0)
	v_mul_f32_e32 v220, v240, v220
	v_mul_f32_e32 v222, v242, v222
	v_mul_f32_e32 v223, v243, v223
	s_cselect_b64 s[0:1], -1, 0
	v_mul_f32_e32 v221, v221, v227
	v_cndmask_b32_e64 v224, v220, 0, s[18:19]
	v_cndmask_b32_e64 v225, v222, 0, s[22:23]
	v_cndmask_b32_e64 v226, v223, 0, s[24:25]
	s_and_b64 s[52:53], s[0:1], s[20:21]
	v_mul_f32_e32 v221, v241, v221
	v_cndmask_b32_e64 v224, 0, v224, s[0:1]
	v_cndmask_b32_e64 v225, 0, v225, s[0:1]
	v_cndmask_b32_e64 v226, 0, v226, s[0:1]
	s_or_b64 s[0:1], vcc, s[52:53]
	v_add_u32_e32 v244, 0, v213
	v_cndmask_b32_e32 v220, v224, v220, vcc
	v_cndmask_b32_e64 v221, 0, v221, s[0:1]
	v_cndmask_b32_e32 v222, v225, v222, vcc
	v_cndmask_b32_e32 v223, v226, v223, vcc
	v_add_u32_e32 v245, 0, v214
	v_add_u32_e32 v246, 0, v215
	v_add_u32_e32 v247, 0, v216
	v_cvt_pk_bf16_f32 v220, v220, v221
	s_nop 1
	v_cvt_pk_bf16_f32 v221, v222, v223
	s_nop 1
	ds_read_b64 v[222:223], v244
	ds_read_b64 v[224:225], v245
	ds_read_b64 v[226:227], v246
	ds_read_b64 v[228:229], v247
	s_xor_b32 s51, s49, 64
	v_add_u32_e32 v230, s51, v170
	v_add_u32_e32 v231, s51, v171
	s_waitcnt lgkmcnt(2)
	v_mfma_f32_16x16x32_bf16 v[94:97], v[218:221], v[222:225], v[94:97]
	v_add_u32_e32 v232, s51, v172
	v_add_u32_e32 v233, s51, v173
	ds_read_b64 v[222:223], v230 offset:8704
	s_waitcnt lgkmcnt(1)
	v_mfma_f32_16x16x32_bf16 v[90:93], v[218:221], v[226:229], v[90:93]
	ds_read_b64 v[224:225], v231 offset:8704
	ds_read_b64 v[226:227], v232 offset:13056
	ds_read_b64 v[228:229], v233 offset:13056
	s_add_i32 s50, s50, 2
	s_add_i32 s49, s49, 64
	s_waitcnt lgkmcnt(2)
	v_mfma_f32_16x16x32_bf16 v[86:89], v[218:221], v[222:225], v[86:89]
	v_add_u32_e32 v217, 0x2200, v217
	v_add_u32_e32 v212, 0x80, v212
	v_add_u32_e32 v216, 64, v216
	s_waitcnt lgkmcnt(0)
	v_mfma_f32_16x16x32_bf16 v[82:85], v[218:221], v[226:229], v[82:85]
	v_add_u32_e32 v215, 64, v215
	v_add_u32_e32 v214, 64, v214
	s_cmp_eq_u32 s87, s50
	v_add_u32_e32 v213, 64, v213
	s_cbranch_scc0 .LBB0_231
	ds_read_b64 v[66:67], v187
	s_cmp_eq_u32 s48, 15
	s_cbranch_scc1 .Lvmk_ssd_last
	s_cmp_lg_u32 s28, 0
	s_cbranch_scc1 .Lvmk_ssd_n10
	s_waitcnt vmcnt(12)
	s_branch .Lvmk_ssd_done
.Lvmk_ssd_n10:
	s_waitcnt vmcnt(10)
	s_branch .Lvmk_ssd_done

.Lvmk_ssd_done:
	v_lshlrev_b32_e32 v75, 16, v6
	v_and_b32_e32 v125, 0xffff0000, v5
	v_lshl_add_u32 v74, s48, 7, v209
	s_waitcnt lgkmcnt(0)
	v_lshlrev_b32_e32 v68, 16, v66
	v_and_b32_e32 v66, 0xffff0000, v66
	v_lshlrev_b32_e32 v69, 16, v67
	v_and_b32_e32 v67, 0xffff0000, v67
	v_fma_f32 v66, v135, v66, v95
	v_fma_f32 v68, v135, v68, v94
	ds_write_b32 v204, v66 offset:272
	v_fma_f32 v66, v135, v69, v96
	v_fmac_f32_e32 v97, v135, v67
	ds_write_b32 v204, v68
	ds_write_b32 v204, v66 offset:544
	ds_write_b32 v204, v97 offset:816
	ds_read_b64 v[66:67], v188
	v_and_b32_e32 v94, 0xffff0000, v3
	v_lshlrev_b32_e32 v95, 16, v4
	v_and_b32_e32 v96, 0xffff0000, v4
	v_lshlrev_b32_e32 v97, 16, v5
	s_waitcnt lgkmcnt(0)
	v_lshlrev_b32_e32 v68, 16, v66
	v_and_b32_e32 v66, 0xffff0000, v66
	v_lshlrev_b32_e32 v69, 16, v67
	v_and_b32_e32 v67, 0xffff0000, v67
	v_fma_f32 v66, v135, v66, v91
	v_fma_f32 v68, v135, v68, v90
	ds_write_b32 v204, v66 offset:336
	v_fma_f32 v66, v135, v69, v92
	v_fmac_f32_e32 v93, v135, v67
	ds_write_b32 v204, v68 offset:64
	ds_write_b32 v204, v66 offset:608
	ds_write_b32 v204, v93 offset:880
	ds_read_b64 v[66:67], v189
	v_and_b32_e32 v90, 0xffff0000, v9
	v_lshlrev_b32_e32 v91, 16, v2
	v_and_b32_e32 v92, 0xffff0000, v2
	v_lshlrev_b32_e32 v93, 16, v3
	s_waitcnt lgkmcnt(0)
	v_lshlrev_b32_e32 v68, 16, v66
	v_and_b32_e32 v66, 0xffff0000, v66
	v_lshlrev_b32_e32 v69, 16, v67
	v_and_b32_e32 v67, 0xffff0000, v67
	v_fma_f32 v66, v135, v66, v87
	v_fma_f32 v68, v135, v68, v86
	ds_write_b32 v204, v66 offset:400
	v_fma_f32 v66, v135, v69, v88
	v_fmac_f32_e32 v89, v135, v67
	ds_write_b32 v204, v68 offset:128
	ds_write_b32 v204, v66 offset:672
	ds_write_b32 v204, v89 offset:944
	ds_read_b64 v[66:67], v190
	v_and_b32_e32 v86, 0xffff0000, v7
	v_lshlrev_b32_e32 v87, 16, v8
	v_and_b32_e32 v88, 0xffff0000, v8
	v_lshlrev_b32_e32 v89, 16, v9
	s_waitcnt lgkmcnt(0)
	v_lshlrev_b32_e32 v68, 16, v66
	v_and_b32_e32 v66, 0xffff0000, v66
	v_lshlrev_b32_e32 v69, 16, v67
	v_and_b32_e32 v67, 0xffff0000, v67
	v_fma_f32 v66, v135, v66, v83
	v_fma_f32 v68, v135, v68, v82
	ds_write_b32 v204, v66 offset:464
	v_fma_f32 v66, v135, v69, v84
	v_fmac_f32_e32 v85, v135, v67
	ds_write_b32 v204, v68 offset:192
	ds_write_b32 v204, v66 offset:736
	ds_write_b32 v204, v85 offset:1008
	ds_read_b128 v[76:79], v205
	ds_read_b128 v[80:83], v205 offset:16
	ds_read_b128 v[70:73], v205 offset:32
	ds_read_b128 v[66:69], v205 offset:48
	v_and_b32_e32 v84, 0xffff0000, v6
	s_waitcnt lgkmcnt(3)
	v_mul_f32_e32 v76, v76, v75
	v_mul_f32_e32 v75, 0xbfb8aa3b, v75
	v_exp_f32_e32 v75, v75
	v_lshlrev_b32_e32 v85, 16, v7
	s_waitcnt lgkmcnt(1)
	v_mul_f32_e32 v70, v70, v91
	v_mul_f32_e32 v71, v71, v92
	v_add_f32_e32 v75, 1.0, v75
	v_rcp_f32_e32 v75, v75
	v_mul_f32_e32 v72, v72, v93
	v_mul_f32_e32 v73, v73, v94
	s_waitcnt lgkmcnt(0)
	v_mul_f32_e32 v66, v66, v95
	v_mul_f32_e32 v76, v75, v76
	v_mul_f32_e32 v75, v77, v84
	v_mul_f32_e32 v77, 0xbfb8aa3b, v84
	v_exp_f32_e32 v77, v77
	s_nop 0
	v_add_f32_e32 v77, 1.0, v77
	v_rcp_f32_e32 v77, v77
	s_nop 0
	v_mul_f32_e32 v77, v77, v75
	v_mul_f32_e32 v75, v78, v85
	v_mul_f32_e32 v78, 0xbfb8aa3b, v85
	v_exp_f32_e32 v78, v78
	s_nop 0
	v_add_f32_e32 v78, 1.0, v78
	v_rcp_f32_e32 v78, v78
	s_nop 0
	v_mul_f32_e32 v78, v78, v75
	v_mul_f32_e32 v75, v79, v86
	v_mul_f32_e32 v79, 0xbfb8aa3b, v86
	v_exp_f32_e32 v79, v79
	v_mul_f32_e32 v86, v77, v77
	v_fmac_f32_e32 v86, v76, v76
	v_fmac_f32_e32 v86, v78, v78
	v_add_f32_e32 v79, 1.0, v79
	v_rcp_f32_e32 v79, v79
	s_nop 0
	v_mul_f32_e32 v79, v79, v75
	v_mul_f32_e32 v75, v80, v87
	v_mul_f32_e32 v80, 0xbfb8aa3b, v87
	v_exp_f32_e32 v80, v80
	v_fmac_f32_e32 v86, v79, v79
	v_xor_b32_e32 v87, 1, v99
	v_add_f32_e32 v80, 1.0, v80
	v_rcp_f32_e32 v80, v80
	s_nop 0
	v_mul_f32_e32 v80, v80, v75
	v_mul_f32_e32 v75, v81, v88
	v_mul_f32_e32 v81, 0xbfb8aa3b, v88
	v_exp_f32_e32 v81, v81
	v_fmac_f32_e32 v86, v80, v80
	v_add_f32_e32 v81, 1.0, v81
	v_rcp_f32_e32 v81, v81
	s_nop 0
	v_mul_f32_e32 v81, v81, v75
	v_mul_f32_e32 v75, v82, v89
	v_mul_f32_e32 v82, 0xbfb8aa3b, v89
	v_exp_f32_e32 v82, v82
	v_fmac_f32_e32 v86, v81, v81
	v_add_f32_e32 v82, 1.0, v82
	v_rcp_f32_e32 v82, v82
	s_nop 0
	v_mul_f32_e32 v82, v82, v75
	v_mul_f32_e32 v75, v83, v90
	v_mul_f32_e32 v83, 0xbfb8aa3b, v90
	v_exp_f32_e32 v83, v83
	v_fmac_f32_e32 v86, v82, v82
	v_add_f32_e32 v83, 1.0, v83
	v_rcp_f32_e32 v83, v83
	s_nop 0
	v_mul_f32_e32 v83, v83, v75
	v_mul_f32_e32 v75, 0xbfb8aa3b, v91
	v_exp_f32_e32 v75, v75
	v_fmac_f32_e32 v86, v83, v83
	v_add_f32_e32 v75, 1.0, v75
	v_rcp_f32_e32 v75, v75
	s_nop 0
	v_mul_f32_e32 v70, v75, v70
	v_mul_f32_e32 v75, 0xbfb8aa3b, v92
	v_exp_f32_e32 v75, v75
	v_fmac_f32_e32 v86, v70, v70
	v_add_f32_e32 v75, 1.0, v75
	v_rcp_f32_e32 v75, v75
	s_nop 0
	v_mul_f32_e32 v71, v75, v71
	v_mul_f32_e32 v75, 0xbfb8aa3b, v93
	v_exp_f32_e32 v75, v75
	v_fmac_f32_e32 v86, v71, v71
	v_add_f32_e32 v75, 1.0, v75
	v_rcp_f32_e32 v75, v75
	s_nop 0
	v_mul_f32_e32 v72, v75, v72
	v_mul_f32_e32 v75, 0xbfb8aa3b, v94
	v_exp_f32_e32 v75, v75
	v_fmac_f32_e32 v86, v72, v72
	v_add_f32_e32 v75, 1.0, v75
	v_rcp_f32_e32 v75, v75
	s_nop 0
	v_mul_f32_e32 v73, v75, v73
	v_mul_f32_e32 v75, 0xbfb8aa3b, v95
	v_exp_f32_e32 v75, v75
	v_fmac_f32_e32 v86, v73, v73
	v_add_f32_e32 v75, 1.0, v75
	v_rcp_f32_e32 v75, v75
	s_nop 0
	v_mul_f32_e32 v84, v75, v66
	v_mul_f32_e32 v66, v67, v96
	v_mul_f32_e32 v67, 0xbfb8aa3b, v96
	v_exp_f32_e32 v67, v67
	v_fmac_f32_e32 v86, v84, v84
	v_ashrrev_i32_e32 v75, 31, v74
	v_add_f32_e32 v67, 1.0, v67
	v_rcp_f32_e32 v67, v67
	s_nop 0
	v_mul_f32_e32 v85, v67, v66
	v_mul_f32_e32 v67, 0xbfb8aa3b, v97
	v_exp_f32_e32 v67, v67
	v_mul_f32_e32 v66, v68, v97
	v_fmac_f32_e32 v86, v85, v85
	v_add_f32_e32 v67, 1.0, v67
	v_rcp_f32_e32 v67, v67
	s_nop 0
	v_mul_f32_e32 v68, v67, v66
	v_mul_f32_e32 v67, 0xbfb8aa3b, v125
	v_exp_f32_e32 v67, v67
	v_mul_f32_e32 v66, v69, v125
	v_fmac_f32_e32 v86, v68, v68
	v_add_f32_e32 v67, 1.0, v67
	v_rcp_f32_e32 v67, v67
	s_nop 0
	v_mul_f32_e32 v69, v67, v66
	v_and_b32_e32 v66, 64, v99
	v_add_u32_e32 v67, 64, v66
	v_cmp_lt_i32_e32 vcc, v87, v67
	v_fmac_f32_e32 v86, v69, v69
	s_nop 0
	v_cndmask_b32_e32 v87, v99, v87, vcc
	v_lshlrev_b32_e32 v212, 2, v87
	ds_bpermute_b32 v87, v212, v86
	s_waitcnt lgkmcnt(0)
	v_add_f32_e32 v86, v86, v87
	v_xor_b32_e32 v87, 2, v99
	v_cmp_lt_i32_e32 vcc, v87, v67
	s_nop 1
	v_cndmask_b32_e32 v87, v99, v87, vcc
	v_lshlrev_b32_e32 v213, 2, v87
	ds_bpermute_b32 v87, v213, v86
	s_and_saveexec_b64 s[0:1], s[26:27]
	s_cbranch_execz .LBB0_234
	v_lshlrev_b64 v[88:89], 7, v[74:75]
	v_lshl_add_u64 v[88:89], s[38:39], 0, v[88:89]
	s_waitcnt lgkmcnt(0)
	v_add_f32_e32 v86, v86, v87
	global_store_dword v[88:89], v86, off

.LBB0_272:
	s_or_b64 exec, exec, s[0:1]
	s_waitcnt lgkmcnt(0)
	ds_read_b128 v[84:87], v214
	s_cmp_eq_u32 s90, 15
	s_cbranch_scc1 .Lvmk_ml_last
	s_cmp_lg_u32 s28, 0
	s_cbranch_scc1 .Lvmk_ml_n10
	s_waitcnt vmcnt(14)
	s_branch .Lvmk_ml_done

.Lvmk_ml_done:
	v_lshlrev_b32_e32 v100, 16, v6
	v_and_b32_e32 v101, 0xffff0000, v6
	v_lshlrev_b32_e32 v102, 16, v7
	v_and_b32_e32 v103, 0xffff0000, v7
	s_waitcnt lgkmcnt(0)
	v_mul_f32_e32 v78, v78, v84
	v_mul_f32_e32 v79, v79, v85
	v_mul_f32_e32 v84, 0xbfb8aa3b, v100
	v_mul_f32_e32 v85, 0xbfb8aa3b, v101
	v_exp_f32_e32 v84, v84
	v_exp_f32_e32 v85, v85
	v_mul_f32_e32 v80, v80, v86
	v_mul_f32_e32 v86, 0xbfb8aa3b, v102
	v_add_f32_e32 v84, 1.0, v84
	v_add_f32_e32 v85, 1.0, v85
	v_rcp_f32_e32 v84, v84
	v_rcp_f32_e32 v85, v85
	v_exp_f32_e32 v86, v86
	v_lshlrev_b32_e32 v104, 16, v8
	v_mul_f32_e32 v78, v84, v78
	v_mul_f32_e32 v79, v85, v79
	v_add_f32_e32 v84, 1.0, v86
	v_mul_f32_e32 v85, 0xbfb8aa3b, v103
	v_mul_f32_e32 v86, 0xbfb8aa3b, v104
	v_exp_f32_e32 v85, v85
	v_exp_f32_e32 v86, v86
	ds_read_b128 v[88:91], v214 offset:16
	ds_read_b128 v[92:95], v214 offset:32
	ds_read_b128 v[96:99], v214 offset:48
	v_lshlrev_b32_e32 v125, 16, v9
	v_add_f32_e32 v85, 1.0, v85
	v_add_f32_e32 v86, 1.0, v86
	v_rcp_f32_e32 v85, v85
	v_rcp_f32_e32 v86, v86
	v_and_b32_e32 v230, 0xffff0000, v9
	v_mul_f32_e32 v81, v81, v87
	s_waitcnt lgkmcnt(2)
	v_mul_f32_e32 v74, v74, v88
	v_mul_f32_e32 v81, v85, v81
	v_mul_f32_e32 v74, v86, v74
	v_mul_f32_e32 v85, 0xbfb8aa3b, v125
	v_mul_f32_e32 v86, 0xbfb8aa3b, v230
	v_exp_f32_e32 v85, v85
	v_exp_f32_e32 v86, v86
	v_and_b32_e32 v105, 0xffff0000, v8
	v_mul_f32_e32 v87, 0xbfb8aa3b, v105
	v_add_f32_e32 v85, 1.0, v85
	v_add_f32_e32 v86, 1.0, v86
	v_rcp_f32_e32 v84, v84
	v_exp_f32_e32 v87, v87
	v_rcp_f32_e32 v85, v85
	v_rcp_f32_e32 v86, v86
	v_lshlrev_b32_e32 v231, 16, v2
	v_and_b32_e32 v232, 0xffff0000, v2
	v_lshlrev_b32_e32 v233, 16, v3
	v_mul_f32_e32 v76, v76, v90
	v_mul_f32_e32 v77, v77, v91
	v_mul_f32_e32 v80, v84, v80
	v_add_f32_e32 v84, 1.0, v87
	v_mul_f32_e32 v87, 0xbfb8aa3b, v231
	v_mul_f32_e32 v76, v85, v76
	v_mul_f32_e32 v77, v86, v77
	v_mul_f32_e32 v85, 0xbfb8aa3b, v232
	v_mul_f32_e32 v86, 0xbfb8aa3b, v233
	v_rcp_f32_e32 v84, v84
	v_exp_f32_e32 v87, v87
	v_exp_f32_e32 v85, v85
	v_exp_f32_e32 v86, v86
	v_and_b32_e32 v234, 0xffff0000, v3
	v_mul_f32_e32 v75, v75, v89
	v_mul_f32_e32 v75, v84, v75
	v_add_f32_e32 v84, 1.0, v87
	v_add_f32_e32 v85, 1.0, v85
	v_add_f32_e32 v86, 1.0, v86
	v_mul_f32_e32 v87, 0xbfb8aa3b, v234
	v_rcp_f32_e32 v84, v84
	v_rcp_f32_e32 v85, v85
	v_rcp_f32_e32 v86, v86
	v_exp_f32_e32 v87, v87
	v_lshlrev_b32_e32 v235, 16, v4
	v_and_b32_e32 v236, 0xffff0000, v4
	s_waitcnt lgkmcnt(1)
	v_mul_f32_e32 v70, v70, v92
	v_mul_f32_e32 v71, v71, v93
	v_mul_f32_e32 v72, v72, v94
	v_mul_f32_e32 v84, v84, v70
	v_mul_f32_e32 v85, v85, v71
	v_mul_f32_e32 v86, v86, v72
	v_add_f32_e32 v70, 1.0, v87
	v_mul_f32_e32 v71, 0xbfb8aa3b, v235
	v_mul_f32_e32 v72, 0xbfb8aa3b, v236
	v_rcp_f32_e32 v70, v70
	v_exp_f32_e32 v71, v71
	v_exp_f32_e32 v72, v72
	v_lshlrev_b32_e32 v237, 16, v5
	v_and_b32_e32 v238, 0xffff0000, v5
	v_mul_f32_e32 v73, v73, v95
	v_mul_f32_e32 v87, v70, v73
	v_add_f32_e32 v70, 1.0, v71
	v_add_f32_e32 v71, 1.0, v72
	v_mul_f32_e32 v72, 0xbfb8aa3b, v237
	v_mul_f32_e32 v73, 0xbfb8aa3b, v238
	v_exp_f32_e32 v72, v72
	v_exp_f32_e32 v73, v73
	v_rcp_f32_e32 v70, v70
	v_rcp_f32_e32 v71, v71
	v_add_f32_e32 v72, 1.0, v72
	v_add_f32_e32 v73, 1.0, v73
	s_waitcnt lgkmcnt(0)
	v_mul_f32_e32 v66, v66, v96
	v_mul_f32_e32 v67, v67, v97
	v_rcp_f32_e32 v72, v72
	v_rcp_f32_e32 v73, v73
	v_mul_f32_e32 v88, v70, v66
	v_mul_f32_e32 v89, v71, v67
	v_lshlrev_b64 v[66:67], 13, v[82:83]
	v_lshl_add_u64 v[66:67], s[38:39], 0, v[66:67]
	v_mul_f32_e32 v68, v68, v98
	v_mul_f32_e32 v69, v69, v99
	v_lshl_add_u64 v[70:71], v[66:67], 0, v[106:107]
	s_mov_b64 s[0:1], 0x4e801000
	v_mul_f32_e32 v90, v72, v68
	v_mul_f32_e32 v91, v73, v69
	v_lshl_add_u64 v[72:73], v[70:71], 0, s[0:1]
	s_mov_b32 s0, 0x4e801000
	v_add_co_u32_e32 v70, vcc, s0, v70
	v_cvt_pk_bf16_f32 v66, v78, v79
	v_cvt_pk_bf16_f32 v67, v80, v81
	v_cvt_pk_bf16_f32 v68, v74, v75
	v_cvt_pk_bf16_f32 v69, v76, v77
	s_nop 1
	v_addc_co_u32_e32 v71, vcc, 0, v71, vcc
	s_andn2_b64 vcc, exec, s[88:89]
	global_store_dwordx4 v[70:71], v[66:69], off
	s_nop 1
	v_cvt_pk_bf16_f32 v66, v84, v85
	v_cvt_pk_bf16_f32 v67, v86, v87
	v_cvt_pk_bf16_f32 v68, v88, v89
	v_cvt_pk_bf16_f32 v69, v90, v91
	global_store_dwordx4 v[72:73], v[66:69], off offset:16
	s_cbranch_vccnz .LBB0_274
	v_lshl_add_u32 v2, s68, 7, v209
	v_mad_i64_i32 v[6:7], s[0:1], v2, s80, v[146:147]
	global_load_dwordx4 v[2:5], v[6:7], off offset:16
	s_nop 0
	global_load_dwordx4 v[6:9], v[6:7], off
